# attention in-loop barrier placed 5 fragments (10 MFMAs) before the end of each 2-tile block
# speedup vs baseline: 1.0095x; 1.0095x over previous
.Lattn_pb1:
	s_waitcnt lgkmcnt(6)
	v_mfma_f32_16x16x32_bf16 v[64:67], v[160:163], v[96:99], 0
	v_exp_f32_e32 v88, v88
	v_mfma_f32_16x16x32_bf16 v[68:71], v[160:163], v[112:115], 0
	v_exp_f32_e32 v92, v92
	ds_read_b128 v[234:237], v209 offset:22528
	s_add_u32 s8, s16, 0x3bc00280
	s_addc_u32 s9, s17, 0
	s_add_u32 s6, s15, 0x23a60000
	s_addc_u32 s7, s14, 0
	s_waitcnt lgkmcnt(6)
	v_mfma_f32_16x16x32_bf16 v[0:3], v[164:167], v[216:219], v[0:3]
	v_cvt_pk_bf16_f32 v242, v80, v81
	v_mfma_f32_16x16x32_bf16 v[4:7], v[164:167], v[238:241], v[4:7]
	v_exp_f32_e32 v89, v89
	ds_read_b128 v[160:163], v201 offset:36864
	s_waitcnt vmcnt(4)
	ds_write_b128 v225, v[136:139] offset:0
	s_waitcnt lgkmcnt(7)
	v_mfma_f32_16x16x32_bf16 v[68:71], v[168:171], v[116:119], v[68:71]
	v_exp_f32_e32 v93, v93
	v_mfma_f32_16x16x32_bf16 v[64:67], v[168:171], v[100:103], v[64:67]
	v_cvt_pk_bf16_f32 v243, v82, v83
	ds_read_b128 v[164:167], v209 offset:24576
	ds_write_b128 v226, v[140:143] offset:0
	s_waitcnt lgkmcnt(8)
	v_mfma_f32_16x16x32_bf16 v[12:15], v[172:175], v[238:241], v[12:15]
	v_exp_f32_e32 v90, v90
	v_mfma_f32_16x16x32_bf16 v[8:11], v[172:175], v[216:219], v[8:11]
	v_exp_f32_e32 v94, v94
	ds_read_b128 v[168:171], v202 offset:36864
	ds_write_b64 v227, v[148:149] offset:49152
	s_waitcnt lgkmcnt(9)
	v_mfma_f32_16x16x32_bf16 v[64:67], v[176:179], v[104:107], v[64:67]
	v_cvt_pk_bf16_f32 v204, v84, v85
	v_mfma_f32_16x16x32_bf16 v[68:71], v[176:179], v[120:123], v[68:71]
	v_exp_f32_e32 v91, v91
	ds_read_b128 v[172:175], v209 offset:26624
	ds_write_b64 v228, v[150:151] offset:49152
	s_waitcnt lgkmcnt(10)
	v_mfma_f32_16x16x32_bf16 v[16:19], v[180:183], v[216:219], v[16:19]
	v_exp_f32_e32 v95, v95
	v_mfma_f32_16x16x32_bf16 v[20:23], v[180:183], v[238:241], v[20:23]
	v_cvt_pk_bf16_f32 v205, v86, v87
	v_add_f32_e32 v220, v220, v88
	ds_read_b128 v[176:179], v203 offset:36864
	ds_write_b64 v229, v[144:145] offset:49152
	s_waitcnt lgkmcnt(11)
	v_mfma_f32_16x16x32_bf16 v[68:71], v[230:233], v[124:127], v[68:71]
	v_add_f32_e32 v221, v221, v92
	v_add_f32_e32 v220, v220, v89
	v_mfma_f32_16x16x32_bf16 v[64:67], v[230:233], v[108:111], v[64:67]
	v_add_f32_e32 v221, v221, v93
	v_cvt_pk_bf16_f32 v244, v88, v89
	ds_read_b128 v[180:183], v209 offset:28672
	ds_write_b64 v184, v[146:147] offset:49152
	s_waitcnt lgkmcnt(12)
	v_mfma_f32_16x16x32_bf16 v[28:31], v[234:237], v[238:241], v[28:31]
	v_cvt_pk_bf16_f32 v245, v90, v91
	v_cvt_pk_bf16_f32 v206, v92, v93
	v_mfma_f32_16x16x32_bf16 v[24:27], v[234:237], v[216:219], v[24:27]
	v_cvt_pk_bf16_f32 v207, v94, v95
	ds_read_b128 v[230:233], v246 offset:36864
	global_load_dwordx4 v[148:151], v198, s[8:9]
	s_waitcnt lgkmcnt(12)
	v_mfma_f32_16x16x32_bf16 v[72:75], v[160:163], v[96:99], 0
	v_add_f32_e32 v220, v220, v90
	v_add_f32_e32 v221, v221, v94
	v_mfma_f32_16x16x32_bf16 v[76:79], v[160:163], v[112:115], 0
	v_add_f32_e32 v220, v220, v91
	v_add_f32_e32 v221, v221, v95
	ds_read_b128 v[234:237], v209 offset:30720
	global_load_dwordx4 v[144:147], v199, s[8:9]
	s_waitcnt lgkmcnt(11)
	v_mfma_f32_16x16x32_bf16 v[32:35], v[164:167], v[216:219], v[32:35]
	v_add_f32_e32 v194, v194, v220
	v_add_f32_e32 v195, v195, v221
	v_mfma_f32_16x16x32_bf16 v[36:39], v[164:167], v[238:241], v[36:39]
	v_exp_f32_e32 v64, v64
	ds_read_b128 v[160:163], v201 offset:40960
	global_load_dwordx4 v[136:139], v196, s[6:7]
	s_waitcnt lgkmcnt(10)
	v_mfma_f32_16x16x32_bf16 v[76:79], v[168:171], v[116:119], v[76:79]
	v_exp_f32_e32 v68, v68
	v_mfma_f32_16x16x32_bf16 v[72:75], v[168:171], v[100:103], v[72:75]
	v_exp_f32_e32 v65, v65
	ds_read_b128 v[164:167], v210 offset:16384
	global_load_dwordx4 v[140:143], v197, s[6:7]
	s_waitcnt lgkmcnt(9)
	v_mfma_f32_16x16x32_bf16 v[44:47], v[172:175], v[238:241], v[44:47]
	v_exp_f32_e32 v69, v69
	v_mfma_f32_16x16x32_bf16 v[40:43], v[172:175], v[216:219], v[40:43]
	v_exp_f32_e32 v66, v66
	ds_read_b128 v[168:171], v202 offset:40960
	s_waitcnt lgkmcnt(8)
	v_mfma_f32_16x16x32_bf16 v[72:75], v[176:179], v[104:107], v[72:75]
	v_exp_f32_e32 v70, v70
	v_mfma_f32_16x16x32_bf16 v[76:79], v[176:179], v[120:123], v[76:79]
	v_exp_f32_e32 v67, v67
	ds_read_b128 v[172:175], v210 offset:18432
	s_waitcnt lgkmcnt(7)
	v_mfma_f32_16x16x32_bf16 v[48:51], v[180:183], v[216:219], v[48:51]
	v_exp_f32_e32 v71, v71
	v_mfma_f32_16x16x32_bf16 v[52:55], v[180:183], v[238:241], v[52:55]
	v_add_f32_e32 v220, v64, v65
	ds_read_b128 v[176:179], v203 offset:40960
	s_waitcnt lgkmcnt(6)
	v_mfma_f32_16x16x32_bf16 v[76:79], v[230:233], v[124:127], v[76:79]
	v_add_f32_e32 v221, v68, v69
	v_mfma_f32_16x16x32_bf16 v[72:75], v[230:233], v[108:111], v[72:75]
	v_add_f32_e32 v220, v220, v66
	ds_read_b128 v[180:183], v210 offset:20480
	s_waitcnt lgkmcnt(6)
	v_mfma_f32_16x16x32_bf16 v[60:63], v[234:237], v[238:241], v[60:63]
	v_add_f32_e32 v221, v221, v70
	v_add_f32_e32 v220, v220, v67
	v_mfma_f32_16x16x32_bf16 v[56:59], v[234:237], v[216:219], v[56:59]
	v_add_f32_e32 v221, v221, v71
	ds_read_b128 v[230:233], v246 offset:40960
	s_waitcnt lgkmcnt(6)
	v_mfma_f32_16x16x32_bf16 v[80:83], v[160:163], v[96:99], 0
	v_exp_f32_e32 v72, v72
	v_mfma_f32_16x16x32_bf16 v[84:87], v[160:163], v[112:115], 0
	v_exp_f32_e32 v76, v76
	ds_read_b128 v[234:237], v210 offset:22528
	s_waitcnt lgkmcnt(6)
	v_mfma_f32_16x16x32_bf16 v[0:3], v[164:167], v[242:245], v[0:3]
	v_exp_f32_e32 v73, v73
	v_mfma_f32_16x16x32_bf16 v[4:7], v[164:167], v[204:207], v[4:7]
	v_exp_f32_e32 v77, v77
	ds_read_b128 v[160:163], v201 offset:45056
	s_waitcnt lgkmcnt(6)
	v_mfma_f32_16x16x32_bf16 v[84:87], v[168:171], v[116:119], v[84:87]
	v_exp_f32_e32 v74, v74
	v_mfma_f32_16x16x32_bf16 v[80:83], v[168:171], v[100:103], v[80:83]
	v_exp_f32_e32 v78, v78
	ds_read_b128 v[164:167], v210 offset:24576
	s_waitcnt lgkmcnt(6)
	v_mfma_f32_16x16x32_bf16 v[12:15], v[172:175], v[204:207], v[12:15]
	v_exp_f32_e32 v75, v75
	v_mfma_f32_16x16x32_bf16 v[8:11], v[172:175], v[242:245], v[8:11]
	v_exp_f32_e32 v79, v79
	ds_read_b128 v[168:171], v202 offset:45056
	s_waitcnt lgkmcnt(6)
	v_mfma_f32_16x16x32_bf16 v[80:83], v[176:179], v[104:107], v[80:83]
	v_add_f32_e32 v220, v220, v72
	v_add_f32_e32 v221, v221, v76
	v_mfma_f32_16x16x32_bf16 v[84:87], v[176:179], v[120:123], v[84:87]
	v_add_f32_e32 v220, v220, v73
	ds_read_b128 v[172:175], v210 offset:26624
	s_waitcnt lgkmcnt(6)
	v_mfma_f32_16x16x32_bf16 v[16:19], v[180:183], v[242:245], v[16:19]
	v_add_f32_e32 v221, v221, v77
	v_add_f32_e32 v220, v220, v74
	v_mfma_f32_16x16x32_bf16 v[20:23], v[180:183], v[204:207], v[20:23]
	v_add_f32_e32 v221, v221, v78
	ds_read_b128 v[176:179], v203 offset:45056
	s_waitcnt lgkmcnt(6)
	v_mfma_f32_16x16x32_bf16 v[84:87], v[230:233], v[124:127], v[84:87]
	v_add_f32_e32 v220, v220, v75
	v_add_f32_e32 v221, v221, v79
	v_mfma_f32_16x16x32_bf16 v[80:83], v[230:233], v[108:111], v[80:83]
	v_cvt_pk_bf16_f32 v216, v64, v65
	ds_read_b128 v[180:183], v210 offset:28672
	s_waitcnt lgkmcnt(6)
	v_mfma_f32_16x16x32_bf16 v[28:31], v[234:237], v[204:207], v[28:31]
	v_cvt_pk_bf16_f32 v217, v66, v67
	v_cvt_pk_bf16_f32 v238, v68, v69
	v_mfma_f32_16x16x32_bf16 v[24:27], v[234:237], v[242:245], v[24:27]
	v_cvt_pk_bf16_f32 v239, v70, v71
	ds_read_b128 v[230:233], v246 offset:45056
	s_waitcnt lgkmcnt(6)
	v_mfma_f32_16x16x32_bf16 v[88:91], v[160:163], v[96:99], 0
	v_exp_f32_e32 v80, v80
	v_mfma_f32_16x16x32_bf16 v[92:95], v[160:163], v[112:115], 0
	v_exp_f32_e32 v84, v84
	ds_read_b128 v[234:237], v210 offset:30720
	s_waitcnt lgkmcnt(6)
	v_mfma_f32_16x16x32_bf16 v[32:35], v[164:167], v[242:245], v[32:35]
	v_exp_f32_e32 v81, v81
	v_mfma_f32_16x16x32_bf16 v[36:39], v[164:167], v[204:207], v[36:39]
	v_exp_f32_e32 v85, v85
	s_waitcnt lgkmcnt(5)
	v_mfma_f32_16x16x32_bf16 v[92:95], v[168:171], v[116:119], v[92:95]
	v_exp_f32_e32 v82, v82
	v_mfma_f32_16x16x32_bf16 v[88:91], v[168:171], v[100:103], v[88:91]
	v_exp_f32_e32 v86, v86
	s_waitcnt lgkmcnt(0)
	s_barrier
	ds_read_b128 v[160:163], v201 offset:49152
	ds_read_b128 v[164:167], v209 offset:32768
	v_mfma_f32_16x16x32_bf16 v[44:47], v[172:175], v[204:207], v[44:47]
	v_exp_f32_e32 v83, v83
	v_mfma_f32_16x16x32_bf16 v[40:43], v[172:175], v[242:245], v[40:43]
	v_exp_f32_e32 v87, v87
	ds_read_b128 v[168:171], v202 offset:49152
	v_mfma_f32_16x16x32_bf16 v[88:91], v[176:179], v[104:107], v[88:91]
	v_add_f32_e32 v220, v220, v80
	v_add_f32_e32 v221, v221, v84
	v_mfma_f32_16x16x32_bf16 v[92:95], v[176:179], v[120:123], v[92:95]
	v_add_f32_e32 v220, v220, v81
	ds_read_b128 v[172:175], v209 offset:34816
	v_mfma_f32_16x16x32_bf16 v[48:51], v[180:183], v[242:245], v[48:51]
	v_add_f32_e32 v221, v221, v85
	v_add_f32_e32 v220, v220, v82
	v_mfma_f32_16x16x32_bf16 v[52:55], v[180:183], v[204:207], v[52:55]
	v_add_f32_e32 v221, v221, v86
	ds_read_b128 v[176:179], v203 offset:49152
	v_mfma_f32_16x16x32_bf16 v[92:95], v[230:233], v[124:127], v[92:95]
	v_add_f32_e32 v220, v220, v83
	v_add_f32_e32 v221, v221, v87
	v_mfma_f32_16x16x32_bf16 v[88:91], v[230:233], v[108:111], v[88:91]
	v_cvt_pk_bf16_f32 v218, v72, v73
	ds_read_b128 v[180:183], v209 offset:36864
	v_mfma_f32_16x16x32_bf16 v[60:63], v[234:237], v[204:207], v[60:63]
	v_cvt_pk_bf16_f32 v219, v74, v75
	v_cvt_pk_bf16_f32 v240, v76, v77
	v_mfma_f32_16x16x32_bf16 v[56:59], v[234:237], v[242:245], v[56:59]
	v_cvt_pk_bf16_f32 v241, v78, v79
	ds_read_b128 v[230:233], v246 offset:49152
	s_cmp_eq_u32 s100, 0
	s_cbranch_scc1 .Lattn_pa2
	s_setprio 1
	s_branch .Lattn_pb2

.Lattn_pb3:
	s_waitcnt lgkmcnt(6)
	v_mfma_f32_16x16x32_bf16 v[64:67], v[160:163], v[96:99], 0
	v_exp_f32_e32 v88, v88
	v_mfma_f32_16x16x32_bf16 v[68:71], v[160:163], v[112:115], 0
	v_exp_f32_e32 v92, v92
	ds_read_b128 v[234:237], v209 offset:55296
	s_add_u32 s8, s16, 0x3bc00380
	s_addc_u32 s9, s17, 0
	s_add_u32 s6, s15, 0x23a80000
	s_addc_u32 s7, s14, 0
	s_waitcnt lgkmcnt(6)
	v_mfma_f32_16x16x32_bf16 v[0:3], v[164:167], v[216:219], v[0:3]
	v_cvt_pk_bf16_f32 v242, v80, v81
	v_mfma_f32_16x16x32_bf16 v[4:7], v[164:167], v[238:241], v[4:7]
	v_exp_f32_e32 v89, v89
	ds_read_b128 v[160:163], v201 offset:4096
	s_waitcnt vmcnt(4)
	ds_write_b128 v225, v[136:139] offset:32768
	s_waitcnt lgkmcnt(7)
	v_mfma_f32_16x16x32_bf16 v[68:71], v[168:171], v[116:119], v[68:71]
	v_exp_f32_e32 v93, v93
	v_mfma_f32_16x16x32_bf16 v[64:67], v[168:171], v[100:103], v[64:67]
	v_cvt_pk_bf16_f32 v243, v82, v83
	ds_read_b128 v[164:167], v209 offset:57344
	ds_write_b128 v226, v[140:143] offset:32768
	s_waitcnt lgkmcnt(8)
	v_mfma_f32_16x16x32_bf16 v[12:15], v[172:175], v[238:241], v[12:15]
	v_exp_f32_e32 v90, v90
	v_mfma_f32_16x16x32_bf16 v[8:11], v[172:175], v[216:219], v[8:11]
	v_exp_f32_e32 v94, v94
	ds_read_b128 v[168:171], v202 offset:4096
	ds_write_b64 v227, v[148:149] offset:16384
	s_waitcnt lgkmcnt(9)
	v_mfma_f32_16x16x32_bf16 v[64:67], v[176:179], v[104:107], v[64:67]
	v_cvt_pk_bf16_f32 v204, v84, v85
	v_mfma_f32_16x16x32_bf16 v[68:71], v[176:179], v[120:123], v[68:71]
	v_exp_f32_e32 v91, v91
	ds_read_b128 v[172:175], v209 offset:59392
	ds_write_b64 v228, v[150:151] offset:16384
	s_waitcnt lgkmcnt(10)
	v_mfma_f32_16x16x32_bf16 v[16:19], v[180:183], v[216:219], v[16:19]
	v_exp_f32_e32 v95, v95
	v_mfma_f32_16x16x32_bf16 v[20:23], v[180:183], v[238:241], v[20:23]
	v_cvt_pk_bf16_f32 v205, v86, v87
	v_add_f32_e32 v220, v220, v88
	ds_read_b128 v[176:179], v203 offset:4096
	ds_write_b64 v229, v[144:145] offset:16384
	s_waitcnt lgkmcnt(11)
	v_mfma_f32_16x16x32_bf16 v[68:71], v[230:233], v[124:127], v[68:71]
	v_add_f32_e32 v221, v221, v92
	v_add_f32_e32 v220, v220, v89
	v_mfma_f32_16x16x32_bf16 v[64:67], v[230:233], v[108:111], v[64:67]
	v_add_f32_e32 v221, v221, v93
	v_cvt_pk_bf16_f32 v244, v88, v89
	ds_read_b128 v[180:183], v209 offset:61440
	ds_write_b64 v184, v[146:147] offset:16384
	s_waitcnt lgkmcnt(12)
	v_mfma_f32_16x16x32_bf16 v[28:31], v[234:237], v[238:241], v[28:31]
	v_cvt_pk_bf16_f32 v245, v90, v91
	v_cvt_pk_bf16_f32 v206, v92, v93
	v_mfma_f32_16x16x32_bf16 v[24:27], v[234:237], v[216:219], v[24:27]
	v_cvt_pk_bf16_f32 v207, v94, v95
	ds_read_b128 v[230:233], v246 offset:4096
	global_load_dwordx4 v[148:151], v198, s[8:9]
	s_waitcnt lgkmcnt(12)
	v_mfma_f32_16x16x32_bf16 v[72:75], v[160:163], v[96:99], 0
	v_add_f32_e32 v220, v220, v90
	v_add_f32_e32 v221, v221, v94
	v_mfma_f32_16x16x32_bf16 v[76:79], v[160:163], v[112:115], 0
	v_add_f32_e32 v220, v220, v91
	v_add_f32_e32 v221, v221, v95
	ds_read_b128 v[234:237], v209 offset:63488
	global_load_dwordx4 v[144:147], v199, s[8:9]
	s_waitcnt lgkmcnt(11)
	v_mfma_f32_16x16x32_bf16 v[32:35], v[164:167], v[216:219], v[32:35]
	v_add_f32_e32 v194, v194, v220
	v_add_f32_e32 v195, v195, v221
	v_mfma_f32_16x16x32_bf16 v[36:39], v[164:167], v[238:241], v[36:39]
	v_exp_f32_e32 v64, v64
	ds_read_b128 v[160:163], v201 offset:8192
	global_load_dwordx4 v[136:139], v196, s[6:7]
	s_waitcnt lgkmcnt(10)
	v_mfma_f32_16x16x32_bf16 v[76:79], v[168:171], v[116:119], v[76:79]
	v_exp_f32_e32 v68, v68
	v_mfma_f32_16x16x32_bf16 v[72:75], v[168:171], v[100:103], v[72:75]
	v_exp_f32_e32 v65, v65
	ds_read_b128 v[164:167], v210 offset:49152
	global_load_dwordx4 v[140:143], v197, s[6:7]
	s_waitcnt lgkmcnt(9)
	v_mfma_f32_16x16x32_bf16 v[44:47], v[172:175], v[238:241], v[44:47]
	v_exp_f32_e32 v69, v69
	v_mfma_f32_16x16x32_bf16 v[40:43], v[172:175], v[216:219], v[40:43]
	v_exp_f32_e32 v66, v66
	ds_read_b128 v[168:171], v202 offset:8192
	s_waitcnt lgkmcnt(8)
	v_mfma_f32_16x16x32_bf16 v[72:75], v[176:179], v[104:107], v[72:75]
	v_exp_f32_e32 v70, v70
	v_mfma_f32_16x16x32_bf16 v[76:79], v[176:179], v[120:123], v[76:79]
	v_exp_f32_e32 v67, v67
	ds_read_b128 v[172:175], v210 offset:51200
	s_waitcnt lgkmcnt(7)
	v_mfma_f32_16x16x32_bf16 v[48:51], v[180:183], v[216:219], v[48:51]
	v_exp_f32_e32 v71, v71
	v_mfma_f32_16x16x32_bf16 v[52:55], v[180:183], v[238:241], v[52:55]
	v_add_f32_e32 v220, v64, v65
	ds_read_b128 v[176:179], v203 offset:8192
	s_waitcnt lgkmcnt(6)
	v_mfma_f32_16x16x32_bf16 v[76:79], v[230:233], v[124:127], v[76:79]
	v_add_f32_e32 v221, v68, v69
	v_mfma_f32_16x16x32_bf16 v[72:75], v[230:233], v[108:111], v[72:75]
	v_add_f32_e32 v220, v220, v66
	ds_read_b128 v[180:183], v210 offset:53248
	s_waitcnt lgkmcnt(6)
	v_mfma_f32_16x16x32_bf16 v[60:63], v[234:237], v[238:241], v[60:63]
	v_add_f32_e32 v221, v221, v70
	v_add_f32_e32 v220, v220, v67
	v_mfma_f32_16x16x32_bf16 v[56:59], v[234:237], v[216:219], v[56:59]
	v_add_f32_e32 v221, v221, v71
	ds_read_b128 v[230:233], v246 offset:8192
	s_waitcnt lgkmcnt(6)
	v_mfma_f32_16x16x32_bf16 v[80:83], v[160:163], v[96:99], 0
	v_exp_f32_e32 v72, v72
	v_mfma_f32_16x16x32_bf16 v[84:87], v[160:163], v[112:115], 0
	v_exp_f32_e32 v76, v76
	ds_read_b128 v[234:237], v210 offset:55296
	s_waitcnt lgkmcnt(6)
	v_mfma_f32_16x16x32_bf16 v[0:3], v[164:167], v[242:245], v[0:3]
	v_exp_f32_e32 v73, v73
	v_mfma_f32_16x16x32_bf16 v[4:7], v[164:167], v[204:207], v[4:7]
	v_exp_f32_e32 v77, v77
	ds_read_b128 v[160:163], v201 offset:12288
	s_waitcnt lgkmcnt(6)
	v_mfma_f32_16x16x32_bf16 v[84:87], v[168:171], v[116:119], v[84:87]
	v_exp_f32_e32 v74, v74
	v_mfma_f32_16x16x32_bf16 v[80:83], v[168:171], v[100:103], v[80:83]
	v_exp_f32_e32 v78, v78
	ds_read_b128 v[164:167], v210 offset:57344
	s_waitcnt lgkmcnt(6)
	v_mfma_f32_16x16x32_bf16 v[12:15], v[172:175], v[204:207], v[12:15]
	v_exp_f32_e32 v75, v75
	v_mfma_f32_16x16x32_bf16 v[8:11], v[172:175], v[242:245], v[8:11]
	v_exp_f32_e32 v79, v79
	ds_read_b128 v[168:171], v202 offset:12288
	s_waitcnt lgkmcnt(6)
	v_mfma_f32_16x16x32_bf16 v[80:83], v[176:179], v[104:107], v[80:83]
	v_add_f32_e32 v220, v220, v72
	v_add_f32_e32 v221, v221, v76
	v_mfma_f32_16x16x32_bf16 v[84:87], v[176:179], v[120:123], v[84:87]
	v_add_f32_e32 v220, v220, v73
	ds_read_b128 v[172:175], v210 offset:59392
	s_add_u32 s10, s10, 0x200
	s_addc_u32 s11, s11, 0
	s_add_u32 s12, s12, 0x40000
	s_addc_u32 s13, s13, 0
	s_add_i32 s4, s4, 4
	s_cmpk_lt_u32 s4, 0x104
	s_cselect_b64 s[6:7], -1, 0
	s_and_b64 s[6:7], s[0:1], s[6:7]
	s_and_b64 vcc, exec, s[6:7]
	s_waitcnt lgkmcnt(6)
	v_mfma_f32_16x16x32_bf16 v[16:19], v[180:183], v[242:245], v[16:19]
	v_add_f32_e32 v221, v221, v77
	v_add_f32_e32 v220, v220, v74
	v_mfma_f32_16x16x32_bf16 v[20:23], v[180:183], v[204:207], v[20:23]
	v_add_f32_e32 v221, v221, v78
	ds_read_b128 v[176:179], v203 offset:12288
	s_waitcnt lgkmcnt(6)
	v_mfma_f32_16x16x32_bf16 v[84:87], v[230:233], v[124:127], v[84:87]
	v_add_f32_e32 v220, v220, v75
	v_add_f32_e32 v221, v221, v79
	v_mfma_f32_16x16x32_bf16 v[80:83], v[230:233], v[108:111], v[80:83]
	v_cvt_pk_bf16_f32 v216, v64, v65
	ds_read_b128 v[180:183], v210 offset:61440
	s_waitcnt lgkmcnt(6)
	v_mfma_f32_16x16x32_bf16 v[28:31], v[234:237], v[204:207], v[28:31]
	v_cvt_pk_bf16_f32 v217, v66, v67
	v_cvt_pk_bf16_f32 v238, v68, v69
	v_mfma_f32_16x16x32_bf16 v[24:27], v[234:237], v[242:245], v[24:27]
	v_cvt_pk_bf16_f32 v239, v70, v71
	ds_read_b128 v[230:233], v246 offset:12288
	s_waitcnt lgkmcnt(6)
	v_mfma_f32_16x16x32_bf16 v[88:91], v[160:163], v[96:99], 0
	v_exp_f32_e32 v80, v80
	v_mfma_f32_16x16x32_bf16 v[92:95], v[160:163], v[112:115], 0
	v_exp_f32_e32 v84, v84
	ds_read_b128 v[234:237], v210 offset:63488
	s_waitcnt lgkmcnt(6)
	v_mfma_f32_16x16x32_bf16 v[32:35], v[164:167], v[242:245], v[32:35]
	v_exp_f32_e32 v81, v81
	v_mfma_f32_16x16x32_bf16 v[36:39], v[164:167], v[204:207], v[36:39]
	v_exp_f32_e32 v85, v85
	s_waitcnt lgkmcnt(5)
	v_mfma_f32_16x16x32_bf16 v[92:95], v[168:171], v[116:119], v[92:95]
	v_exp_f32_e32 v82, v82
	v_mfma_f32_16x16x32_bf16 v[88:91], v[168:171], v[100:103], v[88:91]
	v_exp_f32_e32 v86, v86
	s_waitcnt lgkmcnt(0)
	s_barrier
	ds_read_b128 v[160:163], v201 offset:16384
	ds_read_b128 v[164:167], v209 offset:0
	v_mfma_f32_16x16x32_bf16 v[44:47], v[172:175], v[204:207], v[44:47]
	v_exp_f32_e32 v83, v83
	v_mfma_f32_16x16x32_bf16 v[40:43], v[172:175], v[242:245], v[40:43]
	v_exp_f32_e32 v87, v87
	ds_read_b128 v[168:171], v202 offset:16384
	v_mfma_f32_16x16x32_bf16 v[88:91], v[176:179], v[104:107], v[88:91]
	v_add_f32_e32 v220, v220, v80
	v_add_f32_e32 v221, v221, v84
	v_mfma_f32_16x16x32_bf16 v[92:95], v[176:179], v[120:123], v[92:95]
	v_add_f32_e32 v220, v220, v81
	ds_read_b128 v[172:175], v209 offset:2048
	v_mfma_f32_16x16x32_bf16 v[48:51], v[180:183], v[242:245], v[48:51]
	v_add_f32_e32 v221, v221, v85
	v_add_f32_e32 v220, v220, v82
	v_mfma_f32_16x16x32_bf16 v[52:55], v[180:183], v[204:207], v[52:55]
	v_add_f32_e32 v221, v221, v86
	ds_read_b128 v[176:179], v203 offset:16384
	v_mfma_f32_16x16x32_bf16 v[92:95], v[230:233], v[124:127], v[92:95]
	v_add_f32_e32 v220, v220, v83
	v_add_f32_e32 v221, v221, v87
	v_mfma_f32_16x16x32_bf16 v[88:91], v[230:233], v[108:111], v[88:91]
	v_cvt_pk_bf16_f32 v218, v72, v73
	ds_read_b128 v[180:183], v209 offset:4096
	v_mfma_f32_16x16x32_bf16 v[60:63], v[234:237], v[204:207], v[60:63]
	v_cvt_pk_bf16_f32 v219, v74, v75
	v_cvt_pk_bf16_f32 v240, v76, v77
	v_mfma_f32_16x16x32_bf16 v[56:59], v[234:237], v[242:245], v[56:59]
	v_cvt_pk_bf16_f32 v241, v78, v79
	ds_read_b128 v[230:233], v246 offset:16384
	s_cbranch_vccnz .LBB0_734
	s_setprio 0
	s_waitcnt vmcnt(0)
	s_nop 7
	s_nop 7
	ds_swizzle_b32 v64, v194 offset:swizzle(SWAP,16)
	s_waitcnt lgkmcnt(0)
	v_add_f32_e32 v194, v194, v64
	v_mov_b32_e32 v65, v194
	s_nop 1
	v_permlane32_swap_b32_e32 v194, v65
	v_add_f32_e32 v194, v194, v65
	s_nop 0
	v_rcp_f32_e32 v66, v194
	ds_swizzle_b32 v64, v195 offset:swizzle(SWAP,16)
	s_waitcnt lgkmcnt(0)
	v_add_f32_e32 v195, v195, v64
	v_mov_b32_e32 v65, v195
	s_nop 1
	v_permlane32_swap_b32_e32 v195, v65
	v_add_f32_e32 v195, v195, v65
	s_nop 0
	v_rcp_f32_e32 v67, v195
	v_readlane_b32 s100, v250, 8
	v_mbcnt_lo_u32_b32 v68, -1, 0
	v_mbcnt_hi_u32_b32 v68, -1, v68
	v_and_b32_e32 v69, 15, v68
	v_lshrrev_b32_e32 v70, 4, v68
	s_lshr_b32 s101, s100, 1
	v_add_u32_e32 v69, s101, v69
	v_lshlrev_b32_e32 v69, 12, v69
	v_and_b32_e32 v71, 1, v70
	v_lshlrev_b32_e32 v71, 5, v71
	v_and_b32_e32 v70, 2, v70
	v_lshl_add_u32 v71, v70, 3, v71
	v_add_u32_e32 v70, v69, v71
	v_add_u32_e32 v71, 0x10000, v70
	v_mul_f32_e32 v0, v0, v66
	v_mul_f32_e32 v1, v1, v66
	v_mul_f32_e32 v2, v2, v66
	v_mul_f32_e32 v3, v3, v66
	v_mul_f32_e32 v8, v8, v66
	v_mul_f32_e32 v9, v9, v66
	v_mul_f32_e32 v10, v10, v66
	v_mul_f32_e32 v11, v11, v66
	v_cvt_pk_bf16_f32 v72, v0, v1
	v_cvt_pk_bf16_f32 v73, v2, v3
	v_cvt_pk_bf16_f32 v74, v8, v9
	v_cvt_pk_bf16_f32 v75, v10, v11
	s_nop 1
	v_permlane16_swap_b32_e32 v72, v74
	v_permlane16_swap_b32_e32 v73, v75
	s_nop 1
	global_store_dwordx4 v70, v[72:75], s[58:59] offset:0
	v_mul_f32_e32 v16, v16, v66
	v_mul_f32_e32 v17, v17, v66
	v_mul_f32_e32 v18, v18, v66
	v_mul_f32_e32 v19, v19, v66
	v_mul_f32_e32 v24, v24, v66
	v_mul_f32_e32 v25, v25, v66
	v_mul_f32_e32 v26, v26, v66
	v_mul_f32_e32 v27, v27, v66
	v_cvt_pk_bf16_f32 v76, v16, v17
	v_cvt_pk_bf16_f32 v77, v18, v19
	v_cvt_pk_bf16_f32 v78, v24, v25
	v_cvt_pk_bf16_f32 v79, v26, v27
	s_nop 1
	v_permlane16_swap_b32_e32 v76, v78
	v_permlane16_swap_b32_e32 v77, v79
	s_nop 1
	global_store_dwordx4 v70, v[76:79], s[58:59] offset:64
	v_mul_f32_e32 v32, v32, v66
	v_mul_f32_e32 v33, v33, v66
	v_mul_f32_e32 v34, v34, v66
	v_mul_f32_e32 v35, v35, v66
	v_mul_f32_e32 v40, v40, v66
	v_mul_f32_e32 v41, v41, v66
	v_mul_f32_e32 v42, v42, v66
	v_mul_f32_e32 v43, v43, v66
	v_cvt_pk_bf16_f32 v80, v32, v33
	v_cvt_pk_bf16_f32 v81, v34, v35
	v_cvt_pk_bf16_f32 v82, v40, v41
	v_cvt_pk_bf16_f32 v83, v42, v43
	s_nop 1
	v_permlane16_swap_b32_e32 v80, v82
	v_permlane16_swap_b32_e32 v81, v83
	s_nop 1
	global_store_dwordx4 v70, v[80:83], s[58:59] offset:128
	v_mul_f32_e32 v48, v48, v66
	v_mul_f32_e32 v49, v49, v66
	v_mul_f32_e32 v50, v50, v66
	v_mul_f32_e32 v51, v51, v66
	v_mul_f32_e32 v56, v56, v66
	v_mul_f32_e32 v57, v57, v66
	v_mul_f32_e32 v58, v58, v66
	v_mul_f32_e32 v59, v59, v66
	v_cvt_pk_bf16_f32 v84, v48, v49
	v_cvt_pk_bf16_f32 v85, v50, v51
	v_cvt_pk_bf16_f32 v86, v56, v57
	v_cvt_pk_bf16_f32 v87, v58, v59
	s_nop 1
	v_permlane16_swap_b32_e32 v84, v86
	v_permlane16_swap_b32_e32 v85, v87
	s_nop 1
	global_store_dwordx4 v70, v[84:87], s[58:59] offset:192
	v_mul_f32_e32 v4, v4, v67
	v_mul_f32_e32 v5, v5, v67
	v_mul_f32_e32 v6, v6, v67
	v_mul_f32_e32 v7, v7, v67
	v_mul_f32_e32 v12, v12, v67
	v_mul_f32_e32 v13, v13, v67
	v_mul_f32_e32 v14, v14, v67
	v_mul_f32_e32 v15, v15, v67
	v_cvt_pk_bf16_f32 v88, v4, v5
	v_cvt_pk_bf16_f32 v89, v6, v7
	v_cvt_pk_bf16_f32 v90, v12, v13
	v_cvt_pk_bf16_f32 v91, v14, v15
	s_nop 1
	v_permlane16_swap_b32_e32 v88, v90
	v_permlane16_swap_b32_e32 v89, v91
	s_nop 1
	global_store_dwordx4 v71, v[88:91], s[58:59] offset:0
	v_mul_f32_e32 v20, v20, v67
	v_mul_f32_e32 v21, v21, v67
	v_mul_f32_e32 v22, v22, v67
	v_mul_f32_e32 v23, v23, v67
	v_mul_f32_e32 v28, v28, v67
	v_mul_f32_e32 v29, v29, v67
	v_mul_f32_e32 v30, v30, v67
	v_mul_f32_e32 v31, v31, v67
	v_cvt_pk_bf16_f32 v92, v20, v21
	v_cvt_pk_bf16_f32 v93, v22, v23
	v_cvt_pk_bf16_f32 v94, v28, v29
	v_cvt_pk_bf16_f32 v95, v30, v31
	s_nop 1
	v_permlane16_swap_b32_e32 v92, v94
	v_permlane16_swap_b32_e32 v93, v95
	s_nop 1
	global_store_dwordx4 v71, v[92:95], s[58:59] offset:64
	v_mul_f32_e32 v36, v36, v67
	v_mul_f32_e32 v37, v37, v67
	v_mul_f32_e32 v38, v38, v67
	v_mul_f32_e32 v39, v39, v67
	v_mul_f32_e32 v44, v44, v67
	v_mul_f32_e32 v45, v45, v67
	v_mul_f32_e32 v46, v46, v67
	v_mul_f32_e32 v47, v47, v67
	v_cvt_pk_bf16_f32 v72, v36, v37
	v_cvt_pk_bf16_f32 v73, v38, v39
	v_cvt_pk_bf16_f32 v74, v44, v45
	v_cvt_pk_bf16_f32 v75, v46, v47
	s_nop 1
	v_permlane16_swap_b32_e32 v72, v74
	v_permlane16_swap_b32_e32 v73, v75
	s_nop 1
	global_store_dwordx4 v71, v[72:75], s[58:59] offset:128
	v_mul_f32_e32 v52, v52, v67
	v_mul_f32_e32 v53, v53, v67
	v_mul_f32_e32 v54, v54, v67
	v_mul_f32_e32 v55, v55, v67
	v_mul_f32_e32 v60, v60, v67
	v_mul_f32_e32 v61, v61, v67
	v_mul_f32_e32 v62, v62, v67
	v_mul_f32_e32 v63, v63, v67
	v_cvt_pk_bf16_f32 v76, v52, v53
	v_cvt_pk_bf16_f32 v77, v54, v55
	v_cvt_pk_bf16_f32 v78, v60, v61
	v_cvt_pk_bf16_f32 v79, v62, v63
	s_nop 1
	v_permlane16_swap_b32_e32 v76, v78
	v_permlane16_swap_b32_e32 v77, v79
	s_nop 1
	global_store_dwordx4 v71, v[76:79], s[58:59] offset:192
	s_barrier
